# combine phase: nt cache policy on the once-read y/h row loads and the final f32 output stores
# baseline (speedup 1.0000x reference)
.LBB0_1883:
	s_lshl_b32 s0, s8, 3
	s_add_i32 s0, s0, s91
	s_mov_b32 s4, 24
	s_mov_b32 s2, 23
	s_cmpk_gt_i32 s0, 0x3fff
	s_cbranch_scc1 .LBB0_1886
	s_ashr_i32 s5, s4, 31
	s_lshl_b64 s[4:5], s[4:5], 3
	s_add_u32 s4, s92, s4
	s_addc_u32 s5, s93, s5
	s_load_dwordx2 s[4:5], s[4:5], 0x0
	v_lshlrev_b32_e32 v0, 3, v2
	v_and_b32_e32 v176, 0x1f8, v0
	s_mov_b64 s[34:35], 0x48600000
	s_waitcnt lgkmcnt(0)
	v_mov_b32_e32 v4, 0x8400
	global_load_dword v4, v4, s[4:5] offset:384
	v_mov_b32_e32 v5, 0xa500
	global_load_dword v5, v5, s[4:5] offset:384
	v_mov_b32_e32 v6, 0xc600
	global_load_dword v6, v6, s[4:5] offset:384
	global_load_dword v8, v177, s[4:5] offset:384
	v_mov_b32_e32 v9, 0x2100
	global_load_dword v9, v9, s[4:5] offset:384
	v_mov_b32_e32 v10, 0x4200
	global_load_dword v10, v10, s[4:5] offset:384
	v_mov_b32_e32 v11, 0x6300
	global_load_dword v11, v11, s[4:5] offset:384
	s_add_u32 s18, s4, 0x440000
	s_addc_u32 s19, s5, 0
	s_ashr_i32 s3, s2, 31
	s_lshl_b64 s[2:3], s[2:3], 3
	s_add_u32 s2, s92, s2
	s_addc_u32 s3, s93, s3
	s_load_dwordx2 s[12:13], s[2:3], 0x0
	v_lshl_add_u64 v[0:1], s[4:5], 0, v[176:177]
	v_lshl_add_u64 v[0:1], v[0:1], 0, s[34:35]
	s_waitcnt vmcnt(4)
	v_readfirstlane_b32 s1, v6
	v_readfirstlane_b32 s2, v5
	v_readfirstlane_b32 s3, v4
	s_addk_i32 s3, 0xff
	s_ashr_i32 s28, s3, 8
	s_addk_i32 s2, 0xff
	s_ashr_i32 s29, s2, 8
	s_addk_i32 s1, 0xff
	s_ashr_i32 s30, s1, 8
	s_lshl_b32 s2, s9, 3
	s_waitcnt vmcnt(0)
	v_readfirstlane_b32 s21, v9
	v_readfirstlane_b32 s20, v8
	v_readfirstlane_b32 s22, v10
	s_addk_i32 s20, 0xff
	s_addk_i32 s21, 0xff
	v_readfirstlane_b32 s23, v11
	s_ashr_i32 s20, s20, 8
	s_ashr_i32 s21, s21, 8
	s_addk_i32 s22, 0xff
	s_add_i32 s21, s21, s20
	s_ashr_i32 s22, s22, 8
	s_addk_i32 s23, 0xff
	s_add_i32 s22, s22, s21
	s_ashr_i32 s23, s23, 8
	s_add_i32 s23, s23, s22
	s_add_i32 s28, s28, s23
	s_add_i32 s29, s29, s28
	s_add_i32 s30, s30, s29
	s_add_u32 s31, s4, 0x420000
	s_addc_u32 s33, s5, 0
	s_ashr_i32 s1, s0, 31
	s_lshl_b64 s[34:35], s[0:1], 12
	v_and_b32_e32 v4, 63, v2
	s_add_u32 s4, s4, s34
	v_lshlrev_b32_e32 v176, 3, v4
	s_addc_u32 s5, s5, s35
	v_lshl_add_u64 v[2:3], s[4:5], 0, v[176:177]
	s_mov_b64 s[4:5], 0x2d000000
	s_ashr_i32 s3, s2, 31
	s_lshl_b32 s8, s8, 4
	v_readlane_b32 s34, v254, 53
	v_lshl_add_u64 v[2:3], v[2:3], 0, s[4:5]
	s_lshl_b64 s[4:5], s[2:3], 12
	s_add_i32 s8, s34, s8
	s_lshl_b32 s34, s9, 4
	s_lshl_b64 s[36:37], s[0:1], 13
	s_waitcnt lgkmcnt(0)
	s_add_u32 s12, s12, s36
	v_lshlrev_b32_e32 v176, 4, v4
	s_addc_u32 s13, s13, s37
	v_lshl_add_u64 v[4:5], s[12:13], 0, v[176:177]
	s_mov_b64 s[12:13], 0x1000
	v_lshl_add_u64 v[4:5], v[4:5], 0, s[12:13]
	s_lshl_b64 s[12:13], s[2:3], 13
	s_ashr_i32 s9, s8, 31
	s_lshl_b64 s[36:37], s[8:9], 2
	s_add_u32 s38, s31, s36
	s_addc_u32 s39, s33, s37
	global_load_dwordx2 v[74:75], v177, s[38:39]
	global_load_dwordx2 v[76:77], v[2:3], off nt
	global_load_dwordx2 v[78:79], v[2:3], off offset:512 nt
	global_load_dwordx2 v[80:81], v[2:3], off offset:1024 nt
	global_load_dwordx2 v[82:83], v[2:3], off offset:1536 nt
	global_load_dwordx2 v[84:85], v[2:3], off offset:2048 nt
	global_load_dwordx2 v[86:87], v[2:3], off offset:2560 nt
	global_load_dwordx2 v[88:89], v[2:3], off offset:3072 nt
	global_load_dwordx2 v[90:91], v[2:3], off offset:3584 nt
	s_add_i32 s40, s8, 1
	s_ashr_i32 s41, s40, 31
	s_add_u32 s36, s18, s36
	s_addc_u32 s37, s19, s37
	global_load_dword v92, v177, s[36:37]
	s_lshl_b64 s[38:39], s[40:41], 2
	s_add_u32 s36, s18, s38
	s_addc_u32 s37, s19, s39
	global_load_dword v93, v177, s[36:37]
	v_lshl_add_u64 v[2:3], v[2:3], 0, s[4:5]
	s_waitcnt vmcnt(0)
.LBB0_1885:
	s_waitcnt vmcnt(8)
	v_readfirstlane_b32 s1, v74
	v_readfirstlane_b32 s3, v75
	v_mov_b32_e32 v26, v76
	v_mov_b32_e32 v27, v77
	v_mov_b32_e32 v28, v78
	v_mov_b32_e32 v29, v79
	v_mov_b32_e32 v30, v80
	v_mov_b32_e32 v31, v81
	v_mov_b32_e32 v32, v82
	v_mov_b32_e32 v33, v83
	v_mov_b32_e32 v34, v84
	v_mov_b32_e32 v35, v85
	v_mov_b32_e32 v36, v86
	v_mov_b32_e32 v37, v87
	v_mov_b32_e32 v38, v88
	v_mov_b32_e32 v39, v89
	v_mov_b32_e32 v40, v90
	v_mov_b32_e32 v41, v91
	v_mov_b32_e32 v6, v92
	v_mov_b32_e32 v8, v93
	s_ashr_i32 s9, s1, 14
	s_ashr_i32 s35, s3, 14
	s_cmp_eq_u32 s9, 1
	s_cselect_b32 s36, s20, 0
	s_cmp_eq_u32 s35, 1
	s_cselect_b32 s37, s20, 0
	s_cmp_eq_u32 s9, 2
	s_cselect_b32 s36, s21, s36
	s_cmp_eq_u32 s35, 2
	s_cselect_b32 s37, s21, s37
	s_cmp_eq_u32 s9, 3
	s_cselect_b32 s36, s22, s36
	s_cmp_eq_u32 s35, 3
	s_cselect_b32 s37, s22, s37
	s_cmp_eq_u32 s9, 4
	s_cselect_b32 s36, s23, s36
	s_cmp_eq_u32 s35, 4
	s_cselect_b32 s37, s23, s37
	s_cmp_eq_u32 s9, 5
	s_cselect_b32 s36, s28, s36
	s_cmp_eq_u32 s35, 5
	s_cselect_b32 s37, s28, s37
	s_cmp_eq_u32 s9, 6
	s_cselect_b32 s36, s29, s36
	s_cmp_eq_u32 s35, 6
	s_cselect_b32 s37, s29, s37
	s_cmp_eq_u32 s9, 7
	s_cselect_b32 s9, s30, s36
	s_cmp_eq_u32 s35, 7
	s_cselect_b32 s35, s30, s37
	s_lshl_b32 s9, s9, 8
	s_and_b32 s1, s1, 0x3fff
	s_and_b32 s3, s3, 0x3fff
	s_add_i32 s36, s9, s1
	s_lshl_b32 s1, s35, 8
	s_ashr_i32 s37, s36, 31
	s_add_i32 s38, s1, s3
	s_lshl_b64 s[36:37], s[36:37], 12
	s_ashr_i32 s39, s38, 31
	s_lshl_b64 s[38:39], s[38:39], 12
	v_lshl_add_u64 v[10:11], v[0:1], 0, s[36:37]
	v_lshl_add_u64 v[12:13], v[0:1], 0, s[38:39]
	global_load_dwordx2 v[42:43], v[10:11], off nt
	global_load_dwordx2 v[58:59], v[12:13], off nt
	global_load_dwordx2 v[44:45], v[10:11], off offset:512 nt
	global_load_dwordx2 v[60:61], v[12:13], off offset:512 nt
	global_load_dwordx2 v[46:47], v[10:11], off offset:1024 nt
	global_load_dwordx2 v[62:63], v[12:13], off offset:1024 nt
	global_load_dwordx2 v[48:49], v[10:11], off offset:1536 nt
	global_load_dwordx2 v[64:65], v[12:13], off offset:1536 nt
	global_load_dwordx2 v[50:51], v[10:11], off offset:2048 nt
	global_load_dwordx2 v[66:67], v[12:13], off offset:2048 nt
	global_load_dwordx2 v[52:53], v[10:11], off offset:2560 nt
	global_load_dwordx2 v[68:69], v[12:13], off offset:2560 nt
	global_load_dwordx2 v[54:55], v[10:11], off offset:3072 nt
	global_load_dwordx2 v[70:71], v[12:13], off offset:3072 nt
	global_load_dwordx2 v[56:57], v[10:11], off offset:3584 nt
	global_load_dwordx2 v[72:73], v[12:13], off offset:3584 nt
	s_add_i32 s0, s0, s2
	s_add_i32 s8, s8, s34
	s_ashr_i32 s9, s8, 31
	s_lshl_b64 s[36:37], s[8:9], 2
	s_add_u32 s38, s31, s36
	s_addc_u32 s39, s33, s37
	global_load_dwordx2 v[74:75], v177, s[38:39]
	global_load_dwordx2 v[76:77], v[2:3], off nt
	global_load_dwordx2 v[78:79], v[2:3], off offset:512 nt
	global_load_dwordx2 v[80:81], v[2:3], off offset:1024 nt
	global_load_dwordx2 v[82:83], v[2:3], off offset:1536 nt
	global_load_dwordx2 v[84:85], v[2:3], off offset:2048 nt
	global_load_dwordx2 v[86:87], v[2:3], off offset:2560 nt
	global_load_dwordx2 v[88:89], v[2:3], off offset:3072 nt
	global_load_dwordx2 v[90:91], v[2:3], off offset:3584 nt
	s_add_i32 s40, s8, 1
	s_ashr_i32 s41, s40, 31
	s_add_u32 s36, s18, s36
	s_addc_u32 s37, s19, s37
	global_load_dword v92, v177, s[36:37]
	s_lshl_b64 s[38:39], s[40:41], 2
	s_add_u32 s36, s18, s38
	s_addc_u32 s37, s19, s39
	global_load_dword v93, v177, s[36:37]
	v_lshl_add_u64 v[2:3], v[2:3], 0, s[4:5]
	s_cmpk_lt_i32 s0, 0x4000
	s_waitcnt vmcnt(25)
	v_lshlrev_b32_e32 v20, 16, v26
	v_and_b32_e32 v21, 0xffff0000, v26
	v_lshlrev_b32_e32 v22, 16, v42
	v_and_b32_e32 v23, 0xffff0000, v42
	v_lshlrev_b32_e32 v14, 16, v27
	v_and_b32_e32 v15, 0xffff0000, v27
	v_lshlrev_b32_e32 v16, 16, v43
	v_and_b32_e32 v17, 0xffff0000, v43
	v_lshlrev_b32_e32 v24, 16, v58
	v_and_b32_e32 v25, 0xffff0000, v58
	v_lshlrev_b32_e32 v18, 16, v59
	v_and_b32_e32 v19, 0xffff0000, v59
	v_pk_fma_f32 v[20:21], v[6:7], v[22:23], v[20:21] op_sel_hi:[0,1,1]
	v_pk_fma_f32 v[14:15], v[6:7], v[16:17], v[14:15] op_sel_hi:[0,1,1]
	v_pk_fma_f32 v[16:17], v[8:9], v[18:19], v[14:15] op_sel_hi:[0,1,1]
	v_pk_fma_f32 v[14:15], v[8:9], v[24:25], v[20:21] op_sel_hi:[0,1,1]
	global_store_dwordx4 v[4:5], v[14:17], off offset:-4096 nt
	s_waitcnt vmcnt(24)
	v_lshlrev_b32_e32 v20, 16, v28
	v_and_b32_e32 v21, 0xffff0000, v28
	v_lshlrev_b32_e32 v22, 16, v44
	v_and_b32_e32 v23, 0xffff0000, v44
	v_lshlrev_b32_e32 v14, 16, v29
	v_and_b32_e32 v15, 0xffff0000, v29
	v_lshlrev_b32_e32 v16, 16, v45
	v_and_b32_e32 v17, 0xffff0000, v45
	v_lshlrev_b32_e32 v24, 16, v60
	v_and_b32_e32 v25, 0xffff0000, v60
	v_lshlrev_b32_e32 v18, 16, v61
	v_and_b32_e32 v19, 0xffff0000, v61
	v_pk_fma_f32 v[20:21], v[6:7], v[22:23], v[20:21] op_sel_hi:[0,1,1]
	v_pk_fma_f32 v[14:15], v[6:7], v[16:17], v[14:15] op_sel_hi:[0,1,1]
	v_pk_fma_f32 v[16:17], v[8:9], v[18:19], v[14:15] op_sel_hi:[0,1,1]
	v_pk_fma_f32 v[14:15], v[8:9], v[24:25], v[20:21] op_sel_hi:[0,1,1]
	global_store_dwordx4 v[4:5], v[14:17], off offset:-3072 nt
	s_waitcnt vmcnt(23)
	v_lshlrev_b32_e32 v20, 16, v30
	v_and_b32_e32 v21, 0xffff0000, v30
	v_lshlrev_b32_e32 v22, 16, v46
	v_and_b32_e32 v23, 0xffff0000, v46
	v_lshlrev_b32_e32 v14, 16, v31
	v_and_b32_e32 v15, 0xffff0000, v31
	v_lshlrev_b32_e32 v16, 16, v47
	v_and_b32_e32 v17, 0xffff0000, v47
	v_lshlrev_b32_e32 v24, 16, v62
	v_and_b32_e32 v25, 0xffff0000, v62
	v_lshlrev_b32_e32 v18, 16, v63
	v_and_b32_e32 v19, 0xffff0000, v63
	v_pk_fma_f32 v[20:21], v[6:7], v[22:23], v[20:21] op_sel_hi:[0,1,1]
	v_pk_fma_f32 v[14:15], v[6:7], v[16:17], v[14:15] op_sel_hi:[0,1,1]
	v_pk_fma_f32 v[16:17], v[8:9], v[18:19], v[14:15] op_sel_hi:[0,1,1]
	v_pk_fma_f32 v[14:15], v[8:9], v[24:25], v[20:21] op_sel_hi:[0,1,1]
	global_store_dwordx4 v[4:5], v[14:17], off offset:-2048 nt
	s_waitcnt vmcnt(22)
	v_lshlrev_b32_e32 v20, 16, v32
	v_and_b32_e32 v21, 0xffff0000, v32
	v_lshlrev_b32_e32 v22, 16, v48
	v_and_b32_e32 v23, 0xffff0000, v48
	v_lshlrev_b32_e32 v14, 16, v33
	v_and_b32_e32 v15, 0xffff0000, v33
	v_lshlrev_b32_e32 v16, 16, v49
	v_and_b32_e32 v17, 0xffff0000, v49
	v_lshlrev_b32_e32 v24, 16, v64
	v_and_b32_e32 v25, 0xffff0000, v64
	v_lshlrev_b32_e32 v18, 16, v65
	v_and_b32_e32 v19, 0xffff0000, v65
	v_pk_fma_f32 v[20:21], v[6:7], v[22:23], v[20:21] op_sel_hi:[0,1,1]
	v_pk_fma_f32 v[14:15], v[6:7], v[16:17], v[14:15] op_sel_hi:[0,1,1]
	v_pk_fma_f32 v[16:17], v[8:9], v[18:19], v[14:15] op_sel_hi:[0,1,1]
	v_pk_fma_f32 v[14:15], v[8:9], v[24:25], v[20:21] op_sel_hi:[0,1,1]
	global_store_dwordx4 v[4:5], v[14:17], off offset:-1024 nt
	s_waitcnt vmcnt(21)
	v_lshlrev_b32_e32 v20, 16, v34
	v_and_b32_e32 v21, 0xffff0000, v34
	v_lshlrev_b32_e32 v22, 16, v50
	v_and_b32_e32 v23, 0xffff0000, v50
	v_lshlrev_b32_e32 v14, 16, v35
	v_and_b32_e32 v15, 0xffff0000, v35
	v_lshlrev_b32_e32 v16, 16, v51
	v_and_b32_e32 v17, 0xffff0000, v51
	v_lshlrev_b32_e32 v24, 16, v66
	v_and_b32_e32 v25, 0xffff0000, v66
	v_lshlrev_b32_e32 v18, 16, v67
	v_and_b32_e32 v19, 0xffff0000, v67
	v_pk_fma_f32 v[20:21], v[6:7], v[22:23], v[20:21] op_sel_hi:[0,1,1]
	v_pk_fma_f32 v[14:15], v[6:7], v[16:17], v[14:15] op_sel_hi:[0,1,1]
	v_pk_fma_f32 v[16:17], v[8:9], v[18:19], v[14:15] op_sel_hi:[0,1,1]
	v_pk_fma_f32 v[14:15], v[8:9], v[24:25], v[20:21] op_sel_hi:[0,1,1]
	global_store_dwordx4 v[4:5], v[14:17], off nt
	s_waitcnt vmcnt(20)
	v_lshlrev_b32_e32 v20, 16, v36
	v_and_b32_e32 v21, 0xffff0000, v36
	v_lshlrev_b32_e32 v22, 16, v52
	v_and_b32_e32 v23, 0xffff0000, v52
	v_lshlrev_b32_e32 v14, 16, v37
	v_and_b32_e32 v15, 0xffff0000, v37
	v_lshlrev_b32_e32 v16, 16, v53
	v_and_b32_e32 v17, 0xffff0000, v53
	v_lshlrev_b32_e32 v24, 16, v68
	v_and_b32_e32 v25, 0xffff0000, v68
	v_lshlrev_b32_e32 v18, 16, v69
	v_and_b32_e32 v19, 0xffff0000, v69
	v_pk_fma_f32 v[20:21], v[6:7], v[22:23], v[20:21] op_sel_hi:[0,1,1]
	v_pk_fma_f32 v[14:15], v[6:7], v[16:17], v[14:15] op_sel_hi:[0,1,1]
	v_pk_fma_f32 v[16:17], v[8:9], v[18:19], v[14:15] op_sel_hi:[0,1,1]
	v_pk_fma_f32 v[14:15], v[8:9], v[24:25], v[20:21] op_sel_hi:[0,1,1]
	global_store_dwordx4 v[4:5], v[14:17], off offset:1024 nt
	s_waitcnt vmcnt(19)
	v_lshlrev_b32_e32 v20, 16, v38
	v_and_b32_e32 v21, 0xffff0000, v38
	v_lshlrev_b32_e32 v22, 16, v54
	v_and_b32_e32 v23, 0xffff0000, v54
	v_lshlrev_b32_e32 v14, 16, v39
	v_and_b32_e32 v15, 0xffff0000, v39
	v_lshlrev_b32_e32 v16, 16, v55
	v_and_b32_e32 v17, 0xffff0000, v55
	v_lshlrev_b32_e32 v24, 16, v70
	v_and_b32_e32 v25, 0xffff0000, v70
	v_lshlrev_b32_e32 v18, 16, v71
	v_and_b32_e32 v19, 0xffff0000, v71
	v_pk_fma_f32 v[20:21], v[6:7], v[22:23], v[20:21] op_sel_hi:[0,1,1]
	v_pk_fma_f32 v[14:15], v[6:7], v[16:17], v[14:15] op_sel_hi:[0,1,1]
	v_pk_fma_f32 v[16:17], v[8:9], v[18:19], v[14:15] op_sel_hi:[0,1,1]
	v_pk_fma_f32 v[14:15], v[8:9], v[24:25], v[20:21] op_sel_hi:[0,1,1]
	global_store_dwordx4 v[4:5], v[14:17], off offset:2048 nt
	s_waitcnt vmcnt(18)
	v_lshlrev_b32_e32 v20, 16, v40
	v_and_b32_e32 v21, 0xffff0000, v40
	v_lshlrev_b32_e32 v22, 16, v56
	v_and_b32_e32 v23, 0xffff0000, v56
	v_lshlrev_b32_e32 v14, 16, v41
	v_and_b32_e32 v15, 0xffff0000, v41
	v_lshlrev_b32_e32 v16, 16, v57
	v_and_b32_e32 v17, 0xffff0000, v57
	v_lshlrev_b32_e32 v24, 16, v72
	v_and_b32_e32 v25, 0xffff0000, v72
	v_lshlrev_b32_e32 v18, 16, v73
	v_and_b32_e32 v19, 0xffff0000, v73
	v_pk_fma_f32 v[20:21], v[6:7], v[22:23], v[20:21] op_sel_hi:[0,1,1]
	v_pk_fma_f32 v[14:15], v[6:7], v[16:17], v[14:15] op_sel_hi:[0,1,1]
	v_pk_fma_f32 v[16:17], v[8:9], v[18:19], v[14:15] op_sel_hi:[0,1,1]
	v_pk_fma_f32 v[14:15], v[8:9], v[24:25], v[20:21] op_sel_hi:[0,1,1]
	global_store_dwordx4 v[4:5], v[14:17], off offset:3072 nt
	v_lshl_add_u64 v[4:5], v[4:5], 0, s[12:13]
	s_cbranch_scc1 .LBB0_1885
